# speedup vs baseline: 1.0069x; 1.0069x over previous
.LBB2_132:
	s_load_dwordx8 s[4:11], s[0:1], 0x0
	s_load_dwordx2 s[12:13], s[0:1], 0x20
	s_load_dwordx2 s[34:35], s[0:1], 0x28
	s_lshr_b32 s24, s2, 0
	s_and_b32 s25, s2, 0
	s_mul_i32 s26, s25, 16
	s_add_u32 s27, s26, 16
	v_lshl_or_b32 v55, s24, 14, v0
	s_waitcnt lgkmcnt(0)
	s_mov_b32 s14, 0x61a80
	s_mov_b32 s15, 0xf4240
	s_mov_b32 s16, 0x155cc0
	v_mov_b32_e32 v34, s4
	v_mov_b32_e32 v37, s5
	v_mov_b32_e32 v35, s6
	v_mov_b32_e32 v38, s7
	v_mov_b32_e32 v36, s8
	v_mov_b32_e32 v39, s9
	v_mov_b32_e32 v43, 0
	v_mov_b32_e32 v47, 0
	v_mov_b32_e32 v49, 0x30d40
	v_mov_b32_e32 v50, 0xfff6d840
	v_mov_b32_e32 v48, 0x61a80
	v_mov_b32_e32 v51, 0x61a80
	v_mov_b32_e32 v52, 0xf4240
	v_mov_b32_e32 v53, 0x30d40
	v_mov_b32_e32 v54, 0x61a80
	v_cmp_gt_u32_e64 s[18:19], s14, v55
	v_cmp_gt_u32_e64 s[20:21], s15, v55
	v_cmp_gt_u32_e64 s[22:23], s16, v55
	s_nop 0
	v_cndmask_b32_e64 v44, v36, v35, s[20:21]
	v_cndmask_b32_e64 v44, v44, v34, s[18:19]
	v_cndmask_b32_e64 v45, v39, v38, s[20:21]
	v_cndmask_b32_e64 v45, v45, v37, s[18:19]
	v_cndmask_b32_e64 v42, v50, v49, s[20:21]
	v_cndmask_b32_e64 v42, v42, v48, s[18:19]
	v_add_u32_e32 v42, v42, v55
	v_cndmask_b32_e64 v42, 0, v42, s[22:23]
	v_lshl_add_u64 v[46:47], v[42:43], 2, v[44:45]
	global_load_dword v3, v[46:47], off
	v_cndmask_b32_e64 v42, v52, v51, s[20:21]
	v_cndmask_b32_e64 v42, v42, 0, s[18:19]
	v_sub_u32_e32 v42, v55, v42
	v_cndmask_b32_e64 v42, 0, v42, s[22:23]
	v_lshl_add_u64 v[46:47], v[42:43], 2, v[44:45]
	global_load_dword v2, v[46:47], off
	v_add_u32_e32 v40, 0x400, v55
	v_cmp_gt_u32_e64 s[18:19], s14, v40
	v_cmp_gt_u32_e64 s[20:21], s15, v40
	v_cmp_gt_u32_e64 s[22:23], s16, v40
	s_nop 0
	v_cndmask_b32_e64 v44, v36, v35, s[20:21]
	v_cndmask_b32_e64 v44, v44, v34, s[18:19]
	v_cndmask_b32_e64 v45, v39, v38, s[20:21]
	v_cndmask_b32_e64 v45, v45, v37, s[18:19]
	v_cndmask_b32_e64 v42, v50, v49, s[20:21]
	v_cndmask_b32_e64 v42, v42, v48, s[18:19]
	v_add_u32_e32 v42, v42, v40
	v_cndmask_b32_e64 v42, 0, v42, s[22:23]
	v_lshl_add_u64 v[46:47], v[42:43], 2, v[44:45]
	global_load_dword v5, v[46:47], off
	v_cndmask_b32_e64 v42, v52, v51, s[20:21]
	v_cndmask_b32_e64 v42, v42, 0, s[18:19]
	v_sub_u32_e32 v42, v40, v42
	v_cndmask_b32_e64 v42, 0, v42, s[22:23]
	v_lshl_add_u64 v[46:47], v[42:43], 2, v[44:45]
	global_load_dword v4, v[46:47], off
	v_add_u32_e32 v40, 0x800, v55
	v_cmp_gt_u32_e64 s[18:19], s14, v40
	v_cmp_gt_u32_e64 s[20:21], s15, v40
	v_cmp_gt_u32_e64 s[22:23], s16, v40
	s_nop 0
	v_cndmask_b32_e64 v44, v36, v35, s[20:21]
	v_cndmask_b32_e64 v44, v44, v34, s[18:19]
	v_cndmask_b32_e64 v45, v39, v38, s[20:21]
	v_cndmask_b32_e64 v45, v45, v37, s[18:19]
	v_cndmask_b32_e64 v42, v50, v49, s[20:21]
	v_cndmask_b32_e64 v42, v42, v48, s[18:19]
	v_add_u32_e32 v42, v42, v40
	v_cndmask_b32_e64 v42, 0, v42, s[22:23]
	v_lshl_add_u64 v[46:47], v[42:43], 2, v[44:45]
	global_load_dword v7, v[46:47], off
	v_cndmask_b32_e64 v42, v52, v51, s[20:21]
	v_cndmask_b32_e64 v42, v42, 0, s[18:19]
	v_sub_u32_e32 v42, v40, v42
	v_cndmask_b32_e64 v42, 0, v42, s[22:23]
	v_lshl_add_u64 v[46:47], v[42:43], 2, v[44:45]
	global_load_dword v6, v[46:47], off
	v_add_u32_e32 v40, 0xc00, v55
	v_cmp_gt_u32_e64 s[18:19], s14, v40
	v_cmp_gt_u32_e64 s[20:21], s15, v40
	v_cmp_gt_u32_e64 s[22:23], s16, v40
	s_nop 0
	v_cndmask_b32_e64 v44, v36, v35, s[20:21]
	v_cndmask_b32_e64 v44, v44, v34, s[18:19]
	v_cndmask_b32_e64 v45, v39, v38, s[20:21]
	v_cndmask_b32_e64 v45, v45, v37, s[18:19]
	v_cndmask_b32_e64 v42, v50, v49, s[20:21]
	v_cndmask_b32_e64 v42, v42, v48, s[18:19]
	v_add_u32_e32 v42, v42, v40
	v_cndmask_b32_e64 v42, 0, v42, s[22:23]
	v_lshl_add_u64 v[46:47], v[42:43], 2, v[44:45]
	global_load_dword v9, v[46:47], off
	v_cndmask_b32_e64 v42, v52, v51, s[20:21]
	v_cndmask_b32_e64 v42, v42, 0, s[18:19]
	v_sub_u32_e32 v42, v40, v42
	v_cndmask_b32_e64 v42, 0, v42, s[22:23]
	v_lshl_add_u64 v[46:47], v[42:43], 2, v[44:45]
	global_load_dword v8, v[46:47], off
	v_add_u32_e32 v40, 0x1000, v55
	v_cmp_gt_u32_e64 s[18:19], s14, v40
	v_cmp_gt_u32_e64 s[20:21], s15, v40
	v_cmp_gt_u32_e64 s[22:23], s16, v40
	s_nop 0
	v_cndmask_b32_e64 v44, v36, v35, s[20:21]
	v_cndmask_b32_e64 v44, v44, v34, s[18:19]
	v_cndmask_b32_e64 v45, v39, v38, s[20:21]
	v_cndmask_b32_e64 v45, v45, v37, s[18:19]
	v_cndmask_b32_e64 v42, v50, v49, s[20:21]
	v_cndmask_b32_e64 v42, v42, v48, s[18:19]
	v_add_u32_e32 v42, v42, v40
	v_cndmask_b32_e64 v42, 0, v42, s[22:23]
	v_lshl_add_u64 v[46:47], v[42:43], 2, v[44:45]
	global_load_dword v11, v[46:47], off
	v_cndmask_b32_e64 v42, v52, v51, s[20:21]
	v_cndmask_b32_e64 v42, v42, 0, s[18:19]
	v_sub_u32_e32 v42, v40, v42
	v_cndmask_b32_e64 v42, 0, v42, s[22:23]
	v_lshl_add_u64 v[46:47], v[42:43], 2, v[44:45]
	global_load_dword v10, v[46:47], off
	v_add_u32_e32 v40, 0x1400, v55
	v_cmp_gt_u32_e64 s[18:19], s14, v40
	v_cmp_gt_u32_e64 s[20:21], s15, v40
	v_cmp_gt_u32_e64 s[22:23], s16, v40
	s_nop 0
	v_cndmask_b32_e64 v44, v36, v35, s[20:21]
	v_cndmask_b32_e64 v44, v44, v34, s[18:19]
	v_cndmask_b32_e64 v45, v39, v38, s[20:21]
	v_cndmask_b32_e64 v45, v45, v37, s[18:19]
	v_cndmask_b32_e64 v42, v50, v49, s[20:21]
	v_cndmask_b32_e64 v42, v42, v48, s[18:19]
	v_add_u32_e32 v42, v42, v40
	v_cndmask_b32_e64 v42, 0, v42, s[22:23]
	v_lshl_add_u64 v[46:47], v[42:43], 2, v[44:45]
	global_load_dword v13, v[46:47], off
	v_cndmask_b32_e64 v42, v52, v51, s[20:21]
	v_cndmask_b32_e64 v42, v42, 0, s[18:19]
	v_sub_u32_e32 v42, v40, v42
	v_cndmask_b32_e64 v42, 0, v42, s[22:23]
	v_lshl_add_u64 v[46:47], v[42:43], 2, v[44:45]
	global_load_dword v12, v[46:47], off
	v_add_u32_e32 v40, 0x1800, v55
	v_cmp_gt_u32_e64 s[18:19], s14, v40
	v_cmp_gt_u32_e64 s[20:21], s15, v40
	v_cmp_gt_u32_e64 s[22:23], s16, v40
	s_nop 0
	v_cndmask_b32_e64 v44, v36, v35, s[20:21]
	v_cndmask_b32_e64 v44, v44, v34, s[18:19]
	v_cndmask_b32_e64 v45, v39, v38, s[20:21]
	v_cndmask_b32_e64 v45, v45, v37, s[18:19]
	v_cndmask_b32_e64 v42, v50, v49, s[20:21]
	v_cndmask_b32_e64 v42, v42, v48, s[18:19]
	v_add_u32_e32 v42, v42, v40
	v_cndmask_b32_e64 v42, 0, v42, s[22:23]
	v_lshl_add_u64 v[46:47], v[42:43], 2, v[44:45]
	global_load_dword v15, v[46:47], off
	v_cndmask_b32_e64 v42, v52, v51, s[20:21]
	v_cndmask_b32_e64 v42, v42, 0, s[18:19]
	v_sub_u32_e32 v42, v40, v42
	v_cndmask_b32_e64 v42, 0, v42, s[22:23]
	v_lshl_add_u64 v[46:47], v[42:43], 2, v[44:45]
	global_load_dword v14, v[46:47], off
	v_add_u32_e32 v40, 0x1c00, v55
	v_cmp_gt_u32_e64 s[18:19], s14, v40
	v_cmp_gt_u32_e64 s[20:21], s15, v40
	v_cmp_gt_u32_e64 s[22:23], s16, v40
	s_nop 0
	v_cndmask_b32_e64 v44, v36, v35, s[20:21]
	v_cndmask_b32_e64 v44, v44, v34, s[18:19]
	v_cndmask_b32_e64 v45, v39, v38, s[20:21]
	v_cndmask_b32_e64 v45, v45, v37, s[18:19]
	v_cndmask_b32_e64 v42, v50, v49, s[20:21]
	v_cndmask_b32_e64 v42, v42, v48, s[18:19]
	v_add_u32_e32 v42, v42, v40
	v_cndmask_b32_e64 v42, 0, v42, s[22:23]
	v_lshl_add_u64 v[46:47], v[42:43], 2, v[44:45]
	global_load_dword v17, v[46:47], off
	v_cndmask_b32_e64 v42, v52, v51, s[20:21]
	v_cndmask_b32_e64 v42, v42, 0, s[18:19]
	v_sub_u32_e32 v42, v40, v42
	v_cndmask_b32_e64 v42, 0, v42, s[22:23]
	v_lshl_add_u64 v[46:47], v[42:43], 2, v[44:45]
	global_load_dword v16, v[46:47], off
	v_add_u32_e32 v40, 0x2000, v55
	v_cmp_gt_u32_e64 s[18:19], s14, v40
	v_cmp_gt_u32_e64 s[20:21], s15, v40
	v_cmp_gt_u32_e64 s[22:23], s16, v40
	s_nop 0
	v_cndmask_b32_e64 v44, v36, v35, s[20:21]
	v_cndmask_b32_e64 v44, v44, v34, s[18:19]
	v_cndmask_b32_e64 v45, v39, v38, s[20:21]
	v_cndmask_b32_e64 v45, v45, v37, s[18:19]
	v_cndmask_b32_e64 v42, v50, v49, s[20:21]
	v_cndmask_b32_e64 v42, v42, v48, s[18:19]
	v_add_u32_e32 v42, v42, v40
	v_cndmask_b32_e64 v42, 0, v42, s[22:23]
	v_lshl_add_u64 v[46:47], v[42:43], 2, v[44:45]
	global_load_dword v19, v[46:47], off
	v_cndmask_b32_e64 v42, v52, v51, s[20:21]
	v_cndmask_b32_e64 v42, v42, 0, s[18:19]
	v_sub_u32_e32 v42, v40, v42
	v_cndmask_b32_e64 v42, 0, v42, s[22:23]
	v_lshl_add_u64 v[46:47], v[42:43], 2, v[44:45]
	global_load_dword v18, v[46:47], off
	v_add_u32_e32 v40, 0x2400, v55
	v_cmp_gt_u32_e64 s[18:19], s14, v40
	v_cmp_gt_u32_e64 s[20:21], s15, v40
	v_cmp_gt_u32_e64 s[22:23], s16, v40
	s_nop 0
	v_cndmask_b32_e64 v44, v36, v35, s[20:21]
	v_cndmask_b32_e64 v44, v44, v34, s[18:19]
	v_cndmask_b32_e64 v45, v39, v38, s[20:21]
	v_cndmask_b32_e64 v45, v45, v37, s[18:19]
	v_cndmask_b32_e64 v42, v50, v49, s[20:21]
	v_cndmask_b32_e64 v42, v42, v48, s[18:19]
	v_add_u32_e32 v42, v42, v40
	v_cndmask_b32_e64 v42, 0, v42, s[22:23]
	v_lshl_add_u64 v[46:47], v[42:43], 2, v[44:45]
	global_load_dword v21, v[46:47], off
	v_cndmask_b32_e64 v42, v52, v51, s[20:21]
	v_cndmask_b32_e64 v42, v42, 0, s[18:19]
	v_sub_u32_e32 v42, v40, v42
	v_cndmask_b32_e64 v42, 0, v42, s[22:23]
	v_lshl_add_u64 v[46:47], v[42:43], 2, v[44:45]
	global_load_dword v20, v[46:47], off
	v_add_u32_e32 v40, 0x2800, v55
	v_cmp_gt_u32_e64 s[18:19], s14, v40
	v_cmp_gt_u32_e64 s[20:21], s15, v40
	v_cmp_gt_u32_e64 s[22:23], s16, v40
	s_nop 0
	v_cndmask_b32_e64 v44, v36, v35, s[20:21]
	v_cndmask_b32_e64 v44, v44, v34, s[18:19]
	v_cndmask_b32_e64 v45, v39, v38, s[20:21]
	v_cndmask_b32_e64 v45, v45, v37, s[18:19]
	v_cndmask_b32_e64 v42, v50, v49, s[20:21]
	v_cndmask_b32_e64 v42, v42, v48, s[18:19]
	v_add_u32_e32 v42, v42, v40
	v_cndmask_b32_e64 v42, 0, v42, s[22:23]
	v_lshl_add_u64 v[46:47], v[42:43], 2, v[44:45]
	global_load_dword v23, v[46:47], off
	v_cndmask_b32_e64 v42, v52, v51, s[20:21]
	v_cndmask_b32_e64 v42, v42, 0, s[18:19]
	v_sub_u32_e32 v42, v40, v42
	v_cndmask_b32_e64 v42, 0, v42, s[22:23]
	v_lshl_add_u64 v[46:47], v[42:43], 2, v[44:45]
	global_load_dword v22, v[46:47], off
	v_add_u32_e32 v40, 0x2c00, v55
	v_cmp_gt_u32_e64 s[18:19], s14, v40
	v_cmp_gt_u32_e64 s[20:21], s15, v40
	v_cmp_gt_u32_e64 s[22:23], s16, v40
	s_nop 0
	v_cndmask_b32_e64 v44, v36, v35, s[20:21]
	v_cndmask_b32_e64 v44, v44, v34, s[18:19]
	v_cndmask_b32_e64 v45, v39, v38, s[20:21]
	v_cndmask_b32_e64 v45, v45, v37, s[18:19]
	v_cndmask_b32_e64 v42, v50, v49, s[20:21]
	v_cndmask_b32_e64 v42, v42, v48, s[18:19]
	v_add_u32_e32 v42, v42, v40
	v_cndmask_b32_e64 v42, 0, v42, s[22:23]
	v_lshl_add_u64 v[46:47], v[42:43], 2, v[44:45]
	global_load_dword v25, v[46:47], off
	v_cndmask_b32_e64 v42, v52, v51, s[20:21]
	v_cndmask_b32_e64 v42, v42, 0, s[18:19]
	v_sub_u32_e32 v42, v40, v42
	v_cndmask_b32_e64 v42, 0, v42, s[22:23]
	v_lshl_add_u64 v[46:47], v[42:43], 2, v[44:45]
	global_load_dword v24, v[46:47], off
	v_add_u32_e32 v40, 0x3000, v55
	v_cmp_gt_u32_e64 s[18:19], s14, v40
	v_cmp_gt_u32_e64 s[20:21], s15, v40
	v_cmp_gt_u32_e64 s[22:23], s16, v40
	s_nop 0
	v_cndmask_b32_e64 v44, v36, v35, s[20:21]
	v_cndmask_b32_e64 v44, v44, v34, s[18:19]
	v_cndmask_b32_e64 v45, v39, v38, s[20:21]
	v_cndmask_b32_e64 v45, v45, v37, s[18:19]
	v_cndmask_b32_e64 v42, v50, v49, s[20:21]
	v_cndmask_b32_e64 v42, v42, v48, s[18:19]
	v_add_u32_e32 v42, v42, v40
	v_cndmask_b32_e64 v42, 0, v42, s[22:23]
	v_lshl_add_u64 v[46:47], v[42:43], 2, v[44:45]
	global_load_dword v27, v[46:47], off
	v_cndmask_b32_e64 v42, v52, v51, s[20:21]
	v_cndmask_b32_e64 v42, v42, 0, s[18:19]
	v_sub_u32_e32 v42, v40, v42
	v_cndmask_b32_e64 v42, 0, v42, s[22:23]
	v_lshl_add_u64 v[46:47], v[42:43], 2, v[44:45]
	global_load_dword v26, v[46:47], off
	v_add_u32_e32 v40, 0x3400, v55
	v_cmp_gt_u32_e64 s[18:19], s14, v40
	v_cmp_gt_u32_e64 s[20:21], s15, v40
	v_cmp_gt_u32_e64 s[22:23], s16, v40
	s_nop 0
	v_cndmask_b32_e64 v44, v36, v35, s[20:21]
	v_cndmask_b32_e64 v44, v44, v34, s[18:19]
	v_cndmask_b32_e64 v45, v39, v38, s[20:21]
	v_cndmask_b32_e64 v45, v45, v37, s[18:19]
	v_cndmask_b32_e64 v42, v50, v49, s[20:21]
	v_cndmask_b32_e64 v42, v42, v48, s[18:19]
	v_add_u32_e32 v42, v42, v40
	v_cndmask_b32_e64 v42, 0, v42, s[22:23]
	v_lshl_add_u64 v[46:47], v[42:43], 2, v[44:45]
	global_load_dword v29, v[46:47], off
	v_cndmask_b32_e64 v42, v52, v51, s[20:21]
	v_cndmask_b32_e64 v42, v42, 0, s[18:19]
	v_sub_u32_e32 v42, v40, v42
	v_cndmask_b32_e64 v42, 0, v42, s[22:23]
	v_lshl_add_u64 v[46:47], v[42:43], 2, v[44:45]
	global_load_dword v28, v[46:47], off
	v_add_u32_e32 v40, 0x3800, v55
	v_cmp_gt_u32_e64 s[18:19], s14, v40
	v_cmp_gt_u32_e64 s[20:21], s15, v40
	v_cmp_gt_u32_e64 s[22:23], s16, v40
	s_nop 0
	v_cndmask_b32_e64 v44, v36, v35, s[20:21]
	v_cndmask_b32_e64 v44, v44, v34, s[18:19]
	v_cndmask_b32_e64 v45, v39, v38, s[20:21]
	v_cndmask_b32_e64 v45, v45, v37, s[18:19]
	v_cndmask_b32_e64 v42, v50, v49, s[20:21]
	v_cndmask_b32_e64 v42, v42, v48, s[18:19]
	v_add_u32_e32 v42, v42, v40
	v_cndmask_b32_e64 v42, 0, v42, s[22:23]
	v_lshl_add_u64 v[46:47], v[42:43], 2, v[44:45]
	global_load_dword v31, v[46:47], off
	v_cndmask_b32_e64 v42, v52, v51, s[20:21]
	v_cndmask_b32_e64 v42, v42, 0, s[18:19]
	v_sub_u32_e32 v42, v40, v42
	v_cndmask_b32_e64 v42, 0, v42, s[22:23]
	v_lshl_add_u64 v[46:47], v[42:43], 2, v[44:45]
	global_load_dword v30, v[46:47], off
	v_add_u32_e32 v40, 0x3c00, v55
	v_cmp_gt_u32_e64 s[18:19], s14, v40
	v_cmp_gt_u32_e64 s[20:21], s15, v40
	v_cmp_gt_u32_e64 s[22:23], s16, v40
	s_nop 0
	v_cndmask_b32_e64 v44, v36, v35, s[20:21]
	v_cndmask_b32_e64 v44, v44, v34, s[18:19]
	v_cndmask_b32_e64 v45, v39, v38, s[20:21]
	v_cndmask_b32_e64 v45, v45, v37, s[18:19]
	v_cndmask_b32_e64 v42, v50, v49, s[20:21]
	v_cndmask_b32_e64 v42, v42, v48, s[18:19]
	v_add_u32_e32 v42, v42, v40
	v_cndmask_b32_e64 v42, 0, v42, s[22:23]
	v_lshl_add_u64 v[46:47], v[42:43], 2, v[44:45]
	global_load_dword v33, v[46:47], off
	v_cndmask_b32_e64 v42, v52, v51, s[20:21]
	v_cndmask_b32_e64 v42, v42, 0, s[18:19]
	v_sub_u32_e32 v42, v40, v42
	v_cndmask_b32_e64 v42, 0, v42, s[22:23]
	v_lshl_add_u64 v[46:47], v[42:43], 2, v[44:45]
	global_load_dword v32, v[46:47], off
	v_mov_b32_e32 v34, 0
	v_mov_b32_e32 v35, 0
	v_mov_b32_e32 v36, 0
	v_mov_b32_e32 v37, 0
	v_lshlrev_b32_e32 v38, 3, v0
	v_cmp_gt_u32_e32 vcc, 0x224, v0
	s_and_saveexec_b64 s[36:37], vcc
	s_cbranch_execz .Lsc_nohist
	global_load_dwordx2 v[40:41], v38, s[10:11]
	v_add_u32_e32 v39, 0x1120, v38
	global_load_dwordx2 v[42:43], v39, s[10:11]
	v_add_u32_e32 v39, 0x2240, v38
	global_load_dwordx2 v[44:45], v39, s[10:11]
	v_add_u32_e32 v39, 0x3360, v38
	global_load_dwordx2 v[46:47], v39, s[10:11]
	v_add_u32_e32 v39, 0x4480, v38
	global_load_dwordx2 v[48:49], v39, s[10:11]
	v_add_u32_e32 v39, 0x55a0, v38
	global_load_dwordx2 v[50:51], v39, s[10:11]
	v_add_u32_e32 v39, 0x66c0, v38
	global_load_dwordx2 v[52:53], v39, s[10:11]
	v_add_u32_e32 v39, 0x77e0, v38
	global_load_dwordx2 v[54:55], v39, s[10:11]
	v_add_u32_e32 v39, 0x8900, v38
	global_load_dwordx2 v[56:57], v39, s[10:11]
	v_add_u32_e32 v39, 0x9a20, v38
	global_load_dwordx2 v[58:59], v39, s[10:11]
	v_add_u32_e32 v39, 0xab40, v38
	global_load_dwordx2 v[60:61], v39, s[10:11]
	v_add_u32_e32 v39, 0xbc60, v38
	global_load_dwordx2 v[62:63], v39, s[10:11]
	v_add_u32_e32 v39, 0xcd80, v38
	global_load_dwordx2 v[64:65], v39, s[10:11]
	v_add_u32_e32 v39, 0xdea0, v38
	global_load_dwordx2 v[66:67], v39, s[10:11]
	v_add_u32_e32 v39, 0xefc0, v38
	global_load_dwordx2 v[68:69], v39, s[10:11]
	v_add_u32_e32 v39, 0x100e0, v38
	global_load_dwordx2 v[70:71], v39, s[10:11]
	v_add_u32_e32 v39, 0x11200, v38
	global_load_dwordx2 v[72:73], v39, s[10:11]
	v_add_u32_e32 v39, 0x12320, v38
	global_load_dwordx2 v[74:75], v39, s[10:11]
	v_add_u32_e32 v39, 0x13440, v38
	global_load_dwordx2 v[76:77], v39, s[10:11]
	v_add_u32_e32 v39, 0x14560, v38
	global_load_dwordx2 v[78:79], v39, s[10:11]
	v_add_u32_e32 v39, 0x15680, v38
	global_load_dwordx2 v[80:81], v39, s[10:11]
	v_add_u32_e32 v39, 0x167a0, v38
	global_load_dwordx2 v[82:83], v39, s[10:11]
	v_add_u32_e32 v39, 0x178c0, v38
	global_load_dwordx2 v[84:85], v39, s[10:11]
	v_add_u32_e32 v39, 0x189e0, v38
	global_load_dwordx2 v[86:87], v39, s[10:11]
	s_waitcnt vmcnt(23)
	s_cmp_gt_u32 s24, 0
	s_cselect_b32 s3, 1, 0
	v_add_u32_e32 v34, v34, v40
	v_add_u32_e32 v35, v35, v41
	v_mad_u32_u24 v36, v40, s3, v36
	v_mad_u32_u24 v37, v41, s3, v37
	v_add_u32_e32 v39, 0x19b00, v38
	global_load_dwordx2 v[40:41], v39, s[10:11]
	s_waitcnt vmcnt(23)
	s_cmp_gt_u32 s24, 1
	s_cselect_b32 s3, 1, 0
	v_add_u32_e32 v34, v34, v42
	v_add_u32_e32 v35, v35, v43
	v_mad_u32_u24 v36, v42, s3, v36
	v_mad_u32_u24 v37, v43, s3, v37
	v_add_u32_e32 v39, 0x1ac20, v38
	global_load_dwordx2 v[42:43], v39, s[10:11]
	s_waitcnt vmcnt(23)
	s_cmp_gt_u32 s24, 2
	s_cselect_b32 s3, 1, 0
	v_add_u32_e32 v34, v34, v44
	v_add_u32_e32 v35, v35, v45
	v_mad_u32_u24 v36, v44, s3, v36
	v_mad_u32_u24 v37, v45, s3, v37
	v_add_u32_e32 v39, 0x1bd40, v38
	global_load_dwordx2 v[44:45], v39, s[10:11]
	s_waitcnt vmcnt(23)
	s_cmp_gt_u32 s24, 3
	s_cselect_b32 s3, 1, 0
	v_add_u32_e32 v34, v34, v46
	v_add_u32_e32 v35, v35, v47
	v_mad_u32_u24 v36, v46, s3, v36
	v_mad_u32_u24 v37, v47, s3, v37
	v_add_u32_e32 v39, 0x1ce60, v38
	global_load_dwordx2 v[46:47], v39, s[10:11]
	s_waitcnt vmcnt(23)
	s_cmp_gt_u32 s24, 4
	s_cselect_b32 s3, 1, 0
	v_add_u32_e32 v34, v34, v48
	v_add_u32_e32 v35, v35, v49
	v_mad_u32_u24 v36, v48, s3, v36
	v_mad_u32_u24 v37, v49, s3, v37
	v_add_u32_e32 v39, 0x1df80, v38
	global_load_dwordx2 v[48:49], v39, s[10:11]
	s_waitcnt vmcnt(23)
	s_cmp_gt_u32 s24, 5
	s_cselect_b32 s3, 1, 0
	v_add_u32_e32 v34, v34, v50
	v_add_u32_e32 v35, v35, v51
	v_mad_u32_u24 v36, v50, s3, v36
	v_mad_u32_u24 v37, v51, s3, v37
	v_add_u32_e32 v39, 0x1f0a0, v38
	global_load_dwordx2 v[50:51], v39, s[10:11]
	s_waitcnt vmcnt(23)
	s_cmp_gt_u32 s24, 6
	s_cselect_b32 s3, 1, 0
	v_add_u32_e32 v34, v34, v52
	v_add_u32_e32 v35, v35, v53
	v_mad_u32_u24 v36, v52, s3, v36
	v_mad_u32_u24 v37, v53, s3, v37
	v_add_u32_e32 v39, 0x201c0, v38
	global_load_dwordx2 v[52:53], v39, s[10:11]
	s_waitcnt vmcnt(23)
	s_cmp_gt_u32 s24, 7
	s_cselect_b32 s3, 1, 0
	v_add_u32_e32 v34, v34, v54
	v_add_u32_e32 v35, v35, v55
	v_mad_u32_u24 v36, v54, s3, v36
	v_mad_u32_u24 v37, v55, s3, v37
	v_add_u32_e32 v39, 0x212e0, v38
	global_load_dwordx2 v[54:55], v39, s[10:11]
	s_waitcnt vmcnt(23)
	s_cmp_gt_u32 s24, 8
	s_cselect_b32 s3, 1, 0
	v_add_u32_e32 v34, v34, v56
	v_add_u32_e32 v35, v35, v57
	v_mad_u32_u24 v36, v56, s3, v36
	v_mad_u32_u24 v37, v57, s3, v37
	v_add_u32_e32 v39, 0x22400, v38
	global_load_dwordx2 v[56:57], v39, s[10:11]
	s_waitcnt vmcnt(23)
	s_cmp_gt_u32 s24, 9
	s_cselect_b32 s3, 1, 0
	v_add_u32_e32 v34, v34, v58
	v_add_u32_e32 v35, v35, v59
	v_mad_u32_u24 v36, v58, s3, v36
	v_mad_u32_u24 v37, v59, s3, v37
	v_add_u32_e32 v39, 0x23520, v38
	global_load_dwordx2 v[58:59], v39, s[10:11]
	s_waitcnt vmcnt(23)
	s_cmp_gt_u32 s24, 10
	s_cselect_b32 s3, 1, 0
	v_add_u32_e32 v34, v34, v60
	v_add_u32_e32 v35, v35, v61
	v_mad_u32_u24 v36, v60, s3, v36
	v_mad_u32_u24 v37, v61, s3, v37
	v_add_u32_e32 v39, 0x24640, v38
	global_load_dwordx2 v[60:61], v39, s[10:11]
	s_waitcnt vmcnt(23)
	s_cmp_gt_u32 s24, 11
	s_cselect_b32 s3, 1, 0
	v_add_u32_e32 v34, v34, v62
	v_add_u32_e32 v35, v35, v63
	v_mad_u32_u24 v36, v62, s3, v36
	v_mad_u32_u24 v37, v63, s3, v37
	v_add_u32_e32 v39, 0x25760, v38
	global_load_dwordx2 v[62:63], v39, s[10:11]
	s_waitcnt vmcnt(23)
	s_cmp_gt_u32 s24, 12
	s_cselect_b32 s3, 1, 0
	v_add_u32_e32 v34, v34, v64
	v_add_u32_e32 v35, v35, v65
	v_mad_u32_u24 v36, v64, s3, v36
	v_mad_u32_u24 v37, v65, s3, v37
	v_add_u32_e32 v39, 0x26880, v38
	global_load_dwordx2 v[64:65], v39, s[10:11]
	s_waitcnt vmcnt(23)
	s_cmp_gt_u32 s24, 13
	s_cselect_b32 s3, 1, 0
	v_add_u32_e32 v34, v34, v66
	v_add_u32_e32 v35, v35, v67
	v_mad_u32_u24 v36, v66, s3, v36
	v_mad_u32_u24 v37, v67, s3, v37
	v_add_u32_e32 v39, 0x279a0, v38
	global_load_dwordx2 v[66:67], v39, s[10:11]
	s_waitcnt vmcnt(23)
	s_cmp_gt_u32 s24, 14
	s_cselect_b32 s3, 1, 0
	v_add_u32_e32 v34, v34, v68
	v_add_u32_e32 v35, v35, v69
	v_mad_u32_u24 v36, v68, s3, v36
	v_mad_u32_u24 v37, v69, s3, v37
	v_add_u32_e32 v39, 0x28ac0, v38
	global_load_dwordx2 v[68:69], v39, s[10:11]
	s_waitcnt vmcnt(23)
	s_cmp_gt_u32 s24, 15
	s_cselect_b32 s3, 1, 0
	v_add_u32_e32 v34, v34, v70
	v_add_u32_e32 v35, v35, v71
	v_mad_u32_u24 v36, v70, s3, v36
	v_mad_u32_u24 v37, v71, s3, v37
	v_add_u32_e32 v39, 0x29be0, v38
	global_load_dwordx2 v[70:71], v39, s[10:11]
	s_waitcnt vmcnt(23)
	s_cmp_gt_u32 s24, 16
	s_cselect_b32 s3, 1, 0
	v_add_u32_e32 v34, v34, v72
	v_add_u32_e32 v35, v35, v73
	v_mad_u32_u24 v36, v72, s3, v36
	v_mad_u32_u24 v37, v73, s3, v37
	v_add_u32_e32 v39, 0x2ad00, v38
	global_load_dwordx2 v[72:73], v39, s[10:11]
	s_waitcnt vmcnt(23)
	s_cmp_gt_u32 s24, 17
	s_cselect_b32 s3, 1, 0
	v_add_u32_e32 v34, v34, v74
	v_add_u32_e32 v35, v35, v75
	v_mad_u32_u24 v36, v74, s3, v36
	v_mad_u32_u24 v37, v75, s3, v37
	v_add_u32_e32 v39, 0x2be20, v38
	global_load_dwordx2 v[74:75], v39, s[10:11]
	s_waitcnt vmcnt(23)
	s_cmp_gt_u32 s24, 18
	s_cselect_b32 s3, 1, 0
	v_add_u32_e32 v34, v34, v76
	v_add_u32_e32 v35, v35, v77
	v_mad_u32_u24 v36, v76, s3, v36
	v_mad_u32_u24 v37, v77, s3, v37
	v_add_u32_e32 v39, 0x2cf40, v38
	global_load_dwordx2 v[76:77], v39, s[10:11]
	s_waitcnt vmcnt(23)
	s_cmp_gt_u32 s24, 19
	s_cselect_b32 s3, 1, 0
	v_add_u32_e32 v34, v34, v78
	v_add_u32_e32 v35, v35, v79
	v_mad_u32_u24 v36, v78, s3, v36
	v_mad_u32_u24 v37, v79, s3, v37
	v_add_u32_e32 v39, 0x2e060, v38
	global_load_dwordx2 v[78:79], v39, s[10:11]
	s_waitcnt vmcnt(23)
	s_cmp_gt_u32 s24, 20
	s_cselect_b32 s3, 1, 0
	v_add_u32_e32 v34, v34, v80
	v_add_u32_e32 v35, v35, v81
	v_mad_u32_u24 v36, v80, s3, v36
	v_mad_u32_u24 v37, v81, s3, v37
	v_add_u32_e32 v39, 0x2f180, v38
	global_load_dwordx2 v[80:81], v39, s[10:11]
	s_waitcnt vmcnt(23)
	s_cmp_gt_u32 s24, 21
	s_cselect_b32 s3, 1, 0
	v_add_u32_e32 v34, v34, v82
	v_add_u32_e32 v35, v35, v83
	v_mad_u32_u24 v36, v82, s3, v36
	v_mad_u32_u24 v37, v83, s3, v37
	v_add_u32_e32 v39, 0x302a0, v38
	global_load_dwordx2 v[82:83], v39, s[10:11]
	s_waitcnt vmcnt(23)
	s_cmp_gt_u32 s24, 22
	s_cselect_b32 s3, 1, 0
	v_add_u32_e32 v34, v34, v84
	v_add_u32_e32 v35, v35, v85
	v_mad_u32_u24 v36, v84, s3, v36
	v_mad_u32_u24 v37, v85, s3, v37
	v_add_u32_e32 v39, 0x313c0, v38
	global_load_dwordx2 v[84:85], v39, s[10:11]
	s_waitcnt vmcnt(23)
	s_cmp_gt_u32 s24, 23
	s_cselect_b32 s3, 1, 0
	v_add_u32_e32 v34, v34, v86
	v_add_u32_e32 v35, v35, v87
	v_mad_u32_u24 v36, v86, s3, v36
	v_mad_u32_u24 v37, v87, s3, v37
	v_add_u32_e32 v39, 0x324e0, v38
	global_load_dwordx2 v[86:87], v39, s[10:11]
	s_waitcnt vmcnt(23)
	s_cmp_gt_u32 s24, 24
	s_cselect_b32 s3, 1, 0
	v_add_u32_e32 v34, v34, v40
	v_add_u32_e32 v35, v35, v41
	v_mad_u32_u24 v36, v40, s3, v36
	v_mad_u32_u24 v37, v41, s3, v37
	v_add_u32_e32 v39, 0x33600, v38
	global_load_dwordx2 v[40:41], v39, s[10:11]
	s_waitcnt vmcnt(23)
	s_cmp_gt_u32 s24, 25
	s_cselect_b32 s3, 1, 0
	v_add_u32_e32 v34, v34, v42
	v_add_u32_e32 v35, v35, v43
	v_mad_u32_u24 v36, v42, s3, v36
	v_mad_u32_u24 v37, v43, s3, v37
	v_add_u32_e32 v39, 0x34720, v38
	global_load_dwordx2 v[42:43], v39, s[10:11]
	s_waitcnt vmcnt(23)
	s_cmp_gt_u32 s24, 26
	s_cselect_b32 s3, 1, 0
	v_add_u32_e32 v34, v34, v44
	v_add_u32_e32 v35, v35, v45
	v_mad_u32_u24 v36, v44, s3, v36
	v_mad_u32_u24 v37, v45, s3, v37
	v_add_u32_e32 v39, 0x35840, v38
	global_load_dwordx2 v[44:45], v39, s[10:11]
	s_waitcnt vmcnt(23)
	s_cmp_gt_u32 s24, 27
	s_cselect_b32 s3, 1, 0
	v_add_u32_e32 v34, v34, v46
	v_add_u32_e32 v35, v35, v47
	v_mad_u32_u24 v36, v46, s3, v36
	v_mad_u32_u24 v37, v47, s3, v37
	v_add_u32_e32 v39, 0x36960, v38
	global_load_dwordx2 v[46:47], v39, s[10:11]
	s_waitcnt vmcnt(23)
	s_cmp_gt_u32 s24, 28
	s_cselect_b32 s3, 1, 0
	v_add_u32_e32 v34, v34, v48
	v_add_u32_e32 v35, v35, v49
	v_mad_u32_u24 v36, v48, s3, v36
	v_mad_u32_u24 v37, v49, s3, v37
	v_add_u32_e32 v39, 0x37a80, v38
	global_load_dwordx2 v[48:49], v39, s[10:11]
	s_waitcnt vmcnt(23)
	s_cmp_gt_u32 s24, 29
	s_cselect_b32 s3, 1, 0
	v_add_u32_e32 v34, v34, v50
	v_add_u32_e32 v35, v35, v51
	v_mad_u32_u24 v36, v50, s3, v36
	v_mad_u32_u24 v37, v51, s3, v37
	v_add_u32_e32 v39, 0x38ba0, v38
	global_load_dwordx2 v[50:51], v39, s[10:11]
	s_waitcnt vmcnt(23)
	s_cmp_gt_u32 s24, 30
	s_cselect_b32 s3, 1, 0
	v_add_u32_e32 v34, v34, v52
	v_add_u32_e32 v35, v35, v53
	v_mad_u32_u24 v36, v52, s3, v36
	v_mad_u32_u24 v37, v53, s3, v37
	v_add_u32_e32 v39, 0x39cc0, v38
	global_load_dwordx2 v[52:53], v39, s[10:11]
	s_waitcnt vmcnt(23)
	s_cmp_gt_u32 s24, 31
	s_cselect_b32 s3, 1, 0
	v_add_u32_e32 v34, v34, v54
	v_add_u32_e32 v35, v35, v55
	v_mad_u32_u24 v36, v54, s3, v36
	v_mad_u32_u24 v37, v55, s3, v37
	v_add_u32_e32 v39, 0x3ade0, v38
	global_load_dwordx2 v[54:55], v39, s[10:11]
	s_waitcnt vmcnt(23)
	s_cmp_gt_u32 s24, 32
	s_cselect_b32 s3, 1, 0
	v_add_u32_e32 v34, v34, v56
	v_add_u32_e32 v35, v35, v57
	v_mad_u32_u24 v36, v56, s3, v36
	v_mad_u32_u24 v37, v57, s3, v37
	v_add_u32_e32 v39, 0x3bf00, v38
	global_load_dwordx2 v[56:57], v39, s[10:11]
	s_waitcnt vmcnt(23)
	s_cmp_gt_u32 s24, 33
	s_cselect_b32 s3, 1, 0
	v_add_u32_e32 v34, v34, v58
	v_add_u32_e32 v35, v35, v59
	v_mad_u32_u24 v36, v58, s3, v36
	v_mad_u32_u24 v37, v59, s3, v37
	v_add_u32_e32 v39, 0x3d020, v38
	global_load_dwordx2 v[58:59], v39, s[10:11]
	s_waitcnt vmcnt(23)
	s_cmp_gt_u32 s24, 34
	s_cselect_b32 s3, 1, 0
	v_add_u32_e32 v34, v34, v60
	v_add_u32_e32 v35, v35, v61
	v_mad_u32_u24 v36, v60, s3, v36
	v_mad_u32_u24 v37, v61, s3, v37
	v_add_u32_e32 v39, 0x3e140, v38
	global_load_dwordx2 v[60:61], v39, s[10:11]
	s_waitcnt vmcnt(23)
	s_cmp_gt_u32 s24, 35
	s_cselect_b32 s3, 1, 0
	v_add_u32_e32 v34, v34, v62
	v_add_u32_e32 v35, v35, v63
	v_mad_u32_u24 v36, v62, s3, v36
	v_mad_u32_u24 v37, v63, s3, v37
	v_add_u32_e32 v39, 0x3f260, v38
	global_load_dwordx2 v[62:63], v39, s[10:11]
	s_waitcnt vmcnt(23)
	s_cmp_gt_u32 s24, 36
	s_cselect_b32 s3, 1, 0
	v_add_u32_e32 v34, v34, v64
	v_add_u32_e32 v35, v35, v65
	v_mad_u32_u24 v36, v64, s3, v36
	v_mad_u32_u24 v37, v65, s3, v37
	v_add_u32_e32 v39, 0x40380, v38
	global_load_dwordx2 v[64:65], v39, s[10:11]
	s_waitcnt vmcnt(23)
	s_cmp_gt_u32 s24, 37
	s_cselect_b32 s3, 1, 0
	v_add_u32_e32 v34, v34, v66
	v_add_u32_e32 v35, v35, v67
	v_mad_u32_u24 v36, v66, s3, v36
	v_mad_u32_u24 v37, v67, s3, v37
	v_add_u32_e32 v39, 0x414a0, v38
	global_load_dwordx2 v[66:67], v39, s[10:11]
	s_waitcnt vmcnt(23)
	s_cmp_gt_u32 s24, 38
	s_cselect_b32 s3, 1, 0
	v_add_u32_e32 v34, v34, v68
	v_add_u32_e32 v35, v35, v69
	v_mad_u32_u24 v36, v68, s3, v36
	v_mad_u32_u24 v37, v69, s3, v37
	v_add_u32_e32 v39, 0x425c0, v38
	global_load_dwordx2 v[68:69], v39, s[10:11]
	s_waitcnt vmcnt(23)
	s_cmp_gt_u32 s24, 39
	s_cselect_b32 s3, 1, 0
	v_add_u32_e32 v34, v34, v70
	v_add_u32_e32 v35, v35, v71
	v_mad_u32_u24 v36, v70, s3, v36
	v_mad_u32_u24 v37, v71, s3, v37
	v_add_u32_e32 v39, 0x436e0, v38
	global_load_dwordx2 v[70:71], v39, s[10:11]
	s_waitcnt vmcnt(23)
	s_cmp_gt_u32 s24, 40
	s_cselect_b32 s3, 1, 0
	v_add_u32_e32 v34, v34, v72
	v_add_u32_e32 v35, v35, v73
	v_mad_u32_u24 v36, v72, s3, v36
	v_mad_u32_u24 v37, v73, s3, v37
	v_add_u32_e32 v39, 0x44800, v38
	global_load_dwordx2 v[72:73], v39, s[10:11]
	s_waitcnt vmcnt(23)
	s_cmp_gt_u32 s24, 41
	s_cselect_b32 s3, 1, 0
	v_add_u32_e32 v34, v34, v74
	v_add_u32_e32 v35, v35, v75
	v_mad_u32_u24 v36, v74, s3, v36
	v_mad_u32_u24 v37, v75, s3, v37
	v_add_u32_e32 v39, 0x45920, v38
	global_load_dwordx2 v[74:75], v39, s[10:11]
	s_waitcnt vmcnt(23)
	s_cmp_gt_u32 s24, 42
	s_cselect_b32 s3, 1, 0
	v_add_u32_e32 v34, v34, v76
	v_add_u32_e32 v35, v35, v77
	v_mad_u32_u24 v36, v76, s3, v36
	v_mad_u32_u24 v37, v77, s3, v37
	v_add_u32_e32 v39, 0x46a40, v38
	global_load_dwordx2 v[76:77], v39, s[10:11]
	s_waitcnt vmcnt(23)
	s_cmp_gt_u32 s24, 43
	s_cselect_b32 s3, 1, 0
	v_add_u32_e32 v34, v34, v78
	v_add_u32_e32 v35, v35, v79
	v_mad_u32_u24 v36, v78, s3, v36
	v_mad_u32_u24 v37, v79, s3, v37
	v_add_u32_e32 v39, 0x47b60, v38
	global_load_dwordx2 v[78:79], v39, s[10:11]
	s_waitcnt vmcnt(23)
	s_cmp_gt_u32 s24, 44
	s_cselect_b32 s3, 1, 0
	v_add_u32_e32 v34, v34, v80
	v_add_u32_e32 v35, v35, v81
	v_mad_u32_u24 v36, v80, s3, v36
	v_mad_u32_u24 v37, v81, s3, v37
	v_add_u32_e32 v39, 0x48c80, v38
	global_load_dwordx2 v[80:81], v39, s[10:11]
	s_waitcnt vmcnt(23)
	s_cmp_gt_u32 s24, 45
	s_cselect_b32 s3, 1, 0
	v_add_u32_e32 v34, v34, v82
	v_add_u32_e32 v35, v35, v83
	v_mad_u32_u24 v36, v82, s3, v36
	v_mad_u32_u24 v37, v83, s3, v37
	v_add_u32_e32 v39, 0x49da0, v38
	global_load_dwordx2 v[82:83], v39, s[10:11]
	s_waitcnt vmcnt(23)
	s_cmp_gt_u32 s24, 46
	s_cselect_b32 s3, 1, 0
	v_add_u32_e32 v34, v34, v84
	v_add_u32_e32 v35, v35, v85
	v_mad_u32_u24 v36, v84, s3, v36
	v_mad_u32_u24 v37, v85, s3, v37
	v_add_u32_e32 v39, 0x4aec0, v38
	global_load_dwordx2 v[84:85], v39, s[10:11]
	s_waitcnt vmcnt(23)
	s_cmp_gt_u32 s24, 47
	s_cselect_b32 s3, 1, 0
	v_add_u32_e32 v34, v34, v86
	v_add_u32_e32 v35, v35, v87
	v_mad_u32_u24 v36, v86, s3, v36
	v_mad_u32_u24 v37, v87, s3, v37
	v_add_u32_e32 v39, 0x4bfe0, v38
	global_load_dwordx2 v[86:87], v39, s[10:11]
	s_waitcnt vmcnt(23)
	s_cmp_gt_u32 s24, 48
	s_cselect_b32 s3, 1, 0
	v_add_u32_e32 v34, v34, v40
	v_add_u32_e32 v35, v35, v41
	v_mad_u32_u24 v36, v40, s3, v36
	v_mad_u32_u24 v37, v41, s3, v37
	v_add_u32_e32 v39, 0x4d100, v38
	global_load_dwordx2 v[40:41], v39, s[10:11]
	s_waitcnt vmcnt(23)
	s_cmp_gt_u32 s24, 49
	s_cselect_b32 s3, 1, 0
	v_add_u32_e32 v34, v34, v42
	v_add_u32_e32 v35, v35, v43
	v_mad_u32_u24 v36, v42, s3, v36
	v_mad_u32_u24 v37, v43, s3, v37
	v_add_u32_e32 v39, 0x4e220, v38
	global_load_dwordx2 v[42:43], v39, s[10:11]
	s_waitcnt vmcnt(23)
	s_cmp_gt_u32 s24, 50
	s_cselect_b32 s3, 1, 0
	v_add_u32_e32 v34, v34, v44
	v_add_u32_e32 v35, v35, v45
	v_mad_u32_u24 v36, v44, s3, v36
	v_mad_u32_u24 v37, v45, s3, v37
	v_add_u32_e32 v39, 0x4f340, v38
	global_load_dwordx2 v[44:45], v39, s[10:11]
	s_waitcnt vmcnt(23)
	s_cmp_gt_u32 s24, 51
	s_cselect_b32 s3, 1, 0
	v_add_u32_e32 v34, v34, v46
	v_add_u32_e32 v35, v35, v47
	v_mad_u32_u24 v36, v46, s3, v36
	v_mad_u32_u24 v37, v47, s3, v37
	v_add_u32_e32 v39, 0x50460, v38
	global_load_dwordx2 v[46:47], v39, s[10:11]
	s_waitcnt vmcnt(23)
	s_cmp_gt_u32 s24, 52
	s_cselect_b32 s3, 1, 0
	v_add_u32_e32 v34, v34, v48
	v_add_u32_e32 v35, v35, v49
	v_mad_u32_u24 v36, v48, s3, v36
	v_mad_u32_u24 v37, v49, s3, v37
	v_add_u32_e32 v39, 0x51580, v38
	global_load_dwordx2 v[48:49], v39, s[10:11]
	s_waitcnt vmcnt(23)
	s_cmp_gt_u32 s24, 53
	s_cselect_b32 s3, 1, 0
	v_add_u32_e32 v34, v34, v50
	v_add_u32_e32 v35, v35, v51
	v_mad_u32_u24 v36, v50, s3, v36
	v_mad_u32_u24 v37, v51, s3, v37
	v_add_u32_e32 v39, 0x526a0, v38
	global_load_dwordx2 v[50:51], v39, s[10:11]
	s_waitcnt vmcnt(23)
	s_cmp_gt_u32 s24, 54
	s_cselect_b32 s3, 1, 0
	v_add_u32_e32 v34, v34, v52
	v_add_u32_e32 v35, v35, v53
	v_mad_u32_u24 v36, v52, s3, v36
	v_mad_u32_u24 v37, v53, s3, v37
	v_add_u32_e32 v39, 0x537c0, v38
	global_load_dwordx2 v[52:53], v39, s[10:11]
	s_waitcnt vmcnt(23)
	s_cmp_gt_u32 s24, 55
	s_cselect_b32 s3, 1, 0
	v_add_u32_e32 v34, v34, v54
	v_add_u32_e32 v35, v35, v55
	v_mad_u32_u24 v36, v54, s3, v36
	v_mad_u32_u24 v37, v55, s3, v37
	v_add_u32_e32 v39, 0x548e0, v38
	global_load_dwordx2 v[54:55], v39, s[10:11]
	s_waitcnt vmcnt(23)
	s_cmp_gt_u32 s24, 56
	s_cselect_b32 s3, 1, 0
	v_add_u32_e32 v34, v34, v56
	v_add_u32_e32 v35, v35, v57
	v_mad_u32_u24 v36, v56, s3, v36
	v_mad_u32_u24 v37, v57, s3, v37
	v_add_u32_e32 v39, 0x55a00, v38
	global_load_dwordx2 v[56:57], v39, s[10:11]
	s_waitcnt vmcnt(23)
	s_cmp_gt_u32 s24, 57
	s_cselect_b32 s3, 1, 0
	v_add_u32_e32 v34, v34, v58
	v_add_u32_e32 v35, v35, v59
	v_mad_u32_u24 v36, v58, s3, v36
	v_mad_u32_u24 v37, v59, s3, v37
	v_add_u32_e32 v39, 0x56b20, v38
	global_load_dwordx2 v[58:59], v39, s[10:11]
	s_waitcnt vmcnt(23)
	s_cmp_gt_u32 s24, 58
	s_cselect_b32 s3, 1, 0
	v_add_u32_e32 v34, v34, v60
	v_add_u32_e32 v35, v35, v61
	v_mad_u32_u24 v36, v60, s3, v36
	v_mad_u32_u24 v37, v61, s3, v37
	v_add_u32_e32 v39, 0x57c40, v38
	global_load_dwordx2 v[60:61], v39, s[10:11]
	s_waitcnt vmcnt(23)
	s_cmp_gt_u32 s24, 59
	s_cselect_b32 s3, 1, 0
	v_add_u32_e32 v34, v34, v62
	v_add_u32_e32 v35, v35, v63
	v_mad_u32_u24 v36, v62, s3, v36
	v_mad_u32_u24 v37, v63, s3, v37
	v_add_u32_e32 v39, 0x58d60, v38
	global_load_dwordx2 v[62:63], v39, s[10:11]
	s_waitcnt vmcnt(23)
	s_cmp_gt_u32 s24, 60
	s_cselect_b32 s3, 1, 0
	v_add_u32_e32 v34, v34, v64
	v_add_u32_e32 v35, v35, v65
	v_mad_u32_u24 v36, v64, s3, v36
	v_mad_u32_u24 v37, v65, s3, v37
	v_add_u32_e32 v39, 0x59e80, v38
	global_load_dwordx2 v[64:65], v39, s[10:11]
	s_waitcnt vmcnt(23)
	s_cmp_gt_u32 s24, 61
	s_cselect_b32 s3, 1, 0
	v_add_u32_e32 v34, v34, v66
	v_add_u32_e32 v35, v35, v67
	v_mad_u32_u24 v36, v66, s3, v36
	v_mad_u32_u24 v37, v67, s3, v37
	v_add_u32_e32 v39, 0x5afa0, v38
	global_load_dwordx2 v[66:67], v39, s[10:11]
	s_waitcnt vmcnt(23)
	s_cmp_gt_u32 s24, 62
	s_cselect_b32 s3, 1, 0
	v_add_u32_e32 v34, v34, v68
	v_add_u32_e32 v35, v35, v69
	v_mad_u32_u24 v36, v68, s3, v36
	v_mad_u32_u24 v37, v69, s3, v37
	s_waitcnt vmcnt(22)
	s_cmp_gt_u32 s24, 63
	s_cselect_b32 s3, 1, 0
	v_add_u32_e32 v34, v34, v70
	v_add_u32_e32 v35, v35, v71
	v_mad_u32_u24 v36, v70, s3, v36
	v_mad_u32_u24 v37, v71, s3, v37
	s_waitcnt vmcnt(21)
	s_cmp_gt_u32 s24, 64
	s_cselect_b32 s3, 1, 0
	v_add_u32_e32 v34, v34, v72
	v_add_u32_e32 v35, v35, v73
	v_mad_u32_u24 v36, v72, s3, v36
	v_mad_u32_u24 v37, v73, s3, v37
	s_waitcnt vmcnt(20)
	s_cmp_gt_u32 s24, 65
	s_cselect_b32 s3, 1, 0
	v_add_u32_e32 v34, v34, v74
	v_add_u32_e32 v35, v35, v75
	v_mad_u32_u24 v36, v74, s3, v36
	v_mad_u32_u24 v37, v75, s3, v37
	s_waitcnt vmcnt(19)
	s_cmp_gt_u32 s24, 66
	s_cselect_b32 s3, 1, 0
	v_add_u32_e32 v34, v34, v76
	v_add_u32_e32 v35, v35, v77
	v_mad_u32_u24 v36, v76, s3, v36
	v_mad_u32_u24 v37, v77, s3, v37
	s_waitcnt vmcnt(18)
	s_cmp_gt_u32 s24, 67
	s_cselect_b32 s3, 1, 0
	v_add_u32_e32 v34, v34, v78
	v_add_u32_e32 v35, v35, v79
	v_mad_u32_u24 v36, v78, s3, v36
	v_mad_u32_u24 v37, v79, s3, v37
	s_waitcnt vmcnt(17)
	s_cmp_gt_u32 s24, 68
	s_cselect_b32 s3, 1, 0
	v_add_u32_e32 v34, v34, v80
	v_add_u32_e32 v35, v35, v81
	v_mad_u32_u24 v36, v80, s3, v36
	v_mad_u32_u24 v37, v81, s3, v37
	s_waitcnt vmcnt(16)
	s_cmp_gt_u32 s24, 69
	s_cselect_b32 s3, 1, 0
	v_add_u32_e32 v34, v34, v82
	v_add_u32_e32 v35, v35, v83
	v_mad_u32_u24 v36, v82, s3, v36
	v_mad_u32_u24 v37, v83, s3, v37
	s_waitcnt vmcnt(15)
	s_cmp_gt_u32 s24, 70
	s_cselect_b32 s3, 1, 0
	v_add_u32_e32 v34, v34, v84
	v_add_u32_e32 v35, v35, v85
	v_mad_u32_u24 v36, v84, s3, v36
	v_mad_u32_u24 v37, v85, s3, v37
	s_waitcnt vmcnt(14)
	s_cmp_gt_u32 s24, 71
	s_cselect_b32 s3, 1, 0
	v_add_u32_e32 v34, v34, v86
	v_add_u32_e32 v35, v35, v87
	v_mad_u32_u24 v36, v86, s3, v36
	v_mad_u32_u24 v37, v87, s3, v37
	s_waitcnt vmcnt(13)
	s_cmp_gt_u32 s24, 72
	s_cselect_b32 s3, 1, 0
	v_add_u32_e32 v34, v34, v40
	v_add_u32_e32 v35, v35, v41
	v_mad_u32_u24 v36, v40, s3, v36
	v_mad_u32_u24 v37, v41, s3, v37
	s_waitcnt vmcnt(12)
	s_cmp_gt_u32 s24, 73
	s_cselect_b32 s3, 1, 0
	v_add_u32_e32 v34, v34, v42
	v_add_u32_e32 v35, v35, v43
	v_mad_u32_u24 v36, v42, s3, v36
	v_mad_u32_u24 v37, v43, s3, v37
	s_waitcnt vmcnt(11)
	s_cmp_gt_u32 s24, 74
	s_cselect_b32 s3, 1, 0
	v_add_u32_e32 v34, v34, v44
	v_add_u32_e32 v35, v35, v45
	v_mad_u32_u24 v36, v44, s3, v36
	v_mad_u32_u24 v37, v45, s3, v37
	s_waitcnt vmcnt(10)
	s_cmp_gt_u32 s24, 75
	s_cselect_b32 s3, 1, 0
	v_add_u32_e32 v34, v34, v46
	v_add_u32_e32 v35, v35, v47
	v_mad_u32_u24 v36, v46, s3, v36
	v_mad_u32_u24 v37, v47, s3, v37
	s_waitcnt vmcnt(9)
	s_cmp_gt_u32 s24, 76
	s_cselect_b32 s3, 1, 0
	v_add_u32_e32 v34, v34, v48
	v_add_u32_e32 v35, v35, v49
	v_mad_u32_u24 v36, v48, s3, v36
	v_mad_u32_u24 v37, v49, s3, v37
	s_waitcnt vmcnt(8)
	s_cmp_gt_u32 s24, 77
	s_cselect_b32 s3, 1, 0
	v_add_u32_e32 v34, v34, v50
	v_add_u32_e32 v35, v35, v51
	v_mad_u32_u24 v36, v50, s3, v36
	v_mad_u32_u24 v37, v51, s3, v37
	s_waitcnt vmcnt(7)
	s_cmp_gt_u32 s24, 78
	s_cselect_b32 s3, 1, 0
	v_add_u32_e32 v34, v34, v52
	v_add_u32_e32 v35, v35, v53
	v_mad_u32_u24 v36, v52, s3, v36
	v_mad_u32_u24 v37, v53, s3, v37
	s_waitcnt vmcnt(6)
	s_cmp_gt_u32 s24, 79
	s_cselect_b32 s3, 1, 0
	v_add_u32_e32 v34, v34, v54
	v_add_u32_e32 v35, v35, v55
	v_mad_u32_u24 v36, v54, s3, v36
	v_mad_u32_u24 v37, v55, s3, v37
	s_waitcnt vmcnt(5)
	s_cmp_gt_u32 s24, 80
	s_cselect_b32 s3, 1, 0
	v_add_u32_e32 v34, v34, v56
	v_add_u32_e32 v35, v35, v57
	v_mad_u32_u24 v36, v56, s3, v36
	v_mad_u32_u24 v37, v57, s3, v37
	s_waitcnt vmcnt(4)
	s_cmp_gt_u32 s24, 81
	s_cselect_b32 s3, 1, 0
	v_add_u32_e32 v34, v34, v58
	v_add_u32_e32 v35, v35, v59
	v_mad_u32_u24 v36, v58, s3, v36
	v_mad_u32_u24 v37, v59, s3, v37
	s_waitcnt vmcnt(3)
	s_cmp_gt_u32 s24, 82
	s_cselect_b32 s3, 1, 0
	v_add_u32_e32 v34, v34, v60
	v_add_u32_e32 v35, v35, v61
	v_mad_u32_u24 v36, v60, s3, v36
	v_mad_u32_u24 v37, v61, s3, v37
	s_waitcnt vmcnt(2)
	s_cmp_gt_u32 s24, 83
	s_cselect_b32 s3, 1, 0
	v_add_u32_e32 v34, v34, v62
	v_add_u32_e32 v35, v35, v63
	v_mad_u32_u24 v36, v62, s3, v36
	v_mad_u32_u24 v37, v63, s3, v37
	s_waitcnt vmcnt(1)
	s_cmp_gt_u32 s24, 84
	s_cselect_b32 s3, 1, 0
	v_add_u32_e32 v34, v34, v64
	v_add_u32_e32 v35, v35, v65
	v_mad_u32_u24 v36, v64, s3, v36
	v_mad_u32_u24 v37, v65, s3, v37
	s_waitcnt vmcnt(0)
	s_cmp_gt_u32 s24, 85
	s_cselect_b32 s3, 1, 0
	v_add_u32_e32 v34, v34, v66
	v_add_u32_e32 v35, v35, v67
	v_mad_u32_u24 v36, v66, s3, v36
	v_mad_u32_u24 v37, v67, s3, v37
